# norm1(layer 1): modulation tables loaded in one batch; row X pieces issued up front
# speedup vs baseline: 1.0042x; 1.0042x over previous
.LBB0_254:
	s_lshl_b32 s5, s4, 12
	s_add_i32 s24, s4, 1
	s_add_i32 s25, s5, s13
	s_lshl_b32 s28, s24, 12
	s_cmp_ge_i32 s25, s28
	s_cbranch_scc1 .LBB0_253
	s_ashr_i32 s51, s50, 31
	s_lshl_b64 s[6:7], s[50:51], 4
	s_add_u32 s29, s6, 0x400000
	s_addc_u32 s52, s7, 0
	s_lshl_b64 s[6:7], s[50:51], 11
	s_mul_i32 s20, s4, 0x3000
	v_mov_b32_e32 v87, s7
	v_or_b32_e32 v86, s6, v68
	s_lshl_b64 s[6:7], s[50:51], 12
	s_lshl_b64 s[4:5], s[20:21], 2
	v_or_b32_e32 v88, s6, v0
	s_add_u32 s6, s10, s4
	v_mov_b32_e32 v89, s7
	s_addc_u32 s7, s11, s5
	s_add_u32 s4, s6, 0x30000
	s_addc_u32 s5, s7, 0
	s_add_u32 s8, s6, 0x32000
	s_addc_u32 s9, s7, 0
	v_lshlrev_b32_e32 v171, 2, v68
	s_add_u32 s6, s6, 0xa000
	s_addc_u32 s7, s7, 0
	global_load_dwordx4 v[6:9], v171, s[8:9]
	global_load_dwordx4 v[2:5], v[70:71], off
	global_load_dwordx4 v[14:17], v69, s[8:9]
	global_load_dwordx4 v[10:13], v[72:73], off
	global_load_dwordx4 v[22:25], v164, s[8:9]
	global_load_dwordx4 v[18:21], v[74:75], off
	global_load_dwordx4 v[30:33], v165, s[8:9]
	global_load_dwordx4 v[26:29], v[76:77], off
	global_load_dwordx4 v[38:41], v166, s[8:9]
	global_load_dwordx4 v[34:37], v[78:79], off
	global_load_dwordx4 v[46:49], v167, s[8:9]
	global_load_dwordx4 v[42:45], v[80:81], off
	global_load_dwordx4 v[54:57], v168, s[8:9]
	global_load_dwordx4 v[50:53], v[82:83], off
	global_load_dwordx4 v[62:65], v169, s[8:9]
	global_load_dwordx4 v[58:61], v[84:85], off
	s_waitcnt vmcnt(0)
	v_pk_add_f32 v[8:9], v[8:9], 1.0 op_sel_hi:[1,0]
	v_pk_add_f32 v[6:7], v[6:7], 1.0 op_sel_hi:[1,0]
	v_pk_mul_f32 v[90:91], v[4:5], v[8:9]
	v_pk_mul_f32 v[92:93], v[2:3], v[6:7]
	v_pk_add_f32 v[16:17], v[16:17], 1.0 op_sel_hi:[1,0]
	v_pk_add_f32 v[14:15], v[14:15], 1.0 op_sel_hi:[1,0]
	v_pk_mul_f32 v[94:95], v[12:13], v[16:17]
	v_pk_mul_f32 v[96:97], v[10:11], v[14:15]
	v_pk_add_f32 v[24:25], v[24:25], 1.0 op_sel_hi:[1,0]
	v_pk_add_f32 v[22:23], v[22:23], 1.0 op_sel_hi:[1,0]
	v_pk_mul_f32 v[98:99], v[20:21], v[24:25]
	v_pk_mul_f32 v[100:101], v[18:19], v[22:23]
	v_pk_add_f32 v[32:33], v[32:33], 1.0 op_sel_hi:[1,0]
	v_pk_add_f32 v[30:31], v[30:31], 1.0 op_sel_hi:[1,0]
	v_pk_mul_f32 v[102:103], v[28:29], v[32:33]
	v_pk_mul_f32 v[104:105], v[26:27], v[30:31]
	v_pk_add_f32 v[40:41], v[40:41], 1.0 op_sel_hi:[1,0]
	v_pk_add_f32 v[38:39], v[38:39], 1.0 op_sel_hi:[1,0]
	v_pk_mul_f32 v[106:107], v[36:37], v[40:41]
	v_pk_mul_f32 v[108:109], v[34:35], v[38:39]
	v_pk_add_f32 v[48:49], v[48:49], 1.0 op_sel_hi:[1,0]
	v_pk_add_f32 v[46:47], v[46:47], 1.0 op_sel_hi:[1,0]
	v_pk_mul_f32 v[110:111], v[44:45], v[48:49]
	v_pk_mul_f32 v[112:113], v[42:43], v[46:47]
	v_pk_add_f32 v[56:57], v[56:57], 1.0 op_sel_hi:[1,0]
	v_pk_add_f32 v[54:55], v[54:55], 1.0 op_sel_hi:[1,0]
	v_pk_mul_f32 v[114:115], v[52:53], v[56:57]
	v_pk_mul_f32 v[116:117], v[50:51], v[54:55]
	v_pk_add_f32 v[64:65], v[64:65], 1.0 op_sel_hi:[1,0]
	v_pk_add_f32 v[62:63], v[62:63], 1.0 op_sel_hi:[1,0]
	v_pk_mul_f32 v[118:119], v[60:61], v[64:65]
	v_pk_mul_f32 v[120:121], v[58:59], v[62:63]
	global_load_dwordx4 v[2:5], v171, s[4:5]
	global_load_dwordx4 v[6:9], v171, s[6:7]
	global_load_dwordx4 v[10:13], v69, s[4:5]
	global_load_dwordx4 v[14:17], v69, s[6:7]
	global_load_dwordx4 v[18:21], v164, s[4:5]
	global_load_dwordx4 v[22:25], v164, s[6:7]
	global_load_dwordx4 v[26:29], v165, s[4:5]
	global_load_dwordx4 v[30:33], v165, s[6:7]
	global_load_dwordx4 v[34:37], v166, s[4:5]
	global_load_dwordx4 v[38:41], v166, s[6:7]
	global_load_dwordx4 v[42:45], v167, s[4:5]
	global_load_dwordx4 v[46:49], v167, s[6:7]
	global_load_dwordx4 v[50:53], v168, s[4:5]
	global_load_dwordx4 v[54:57], v168, s[6:7]
	global_load_dwordx4 v[58:61], v169, s[4:5]
	global_load_dwordx4 v[62:65], v169, s[6:7]
.LBB0_256:
	s_add_u32 s4, s46, s29
	s_addc_u32 s5, s47, s52
	global_load_dwordx4 v[126:129], v1, s[4:5] nt
	v_lshl_add_u64 v[124:125], s[46:47], 0, v[88:89]
	v_add_co_u32_e32 v150, vcc, 0x11100000, v124
	v_lshl_add_u64 v[122:123], s[46:47], 0, v[86:87]
	s_nop 0
	v_addc_co_u32_e32 v151, vcc, 0, v125, vcc
	global_load_dwordx2 v[124:125], v[150:151], off nt
	global_load_dwordx2 v[202:203], v[150:151], off offset:512 nt
	global_load_dwordx2 v[204:205], v[150:151], off offset:1024 nt
	global_load_dwordx2 v[206:207], v[150:151], off offset:1536 nt
	global_load_dwordx2 v[208:209], v[150:151], off offset:2048 nt
	global_load_dwordx2 v[210:211], v[150:151], off offset:2560 nt
	global_load_dwordx2 v[212:213], v[150:151], off offset:3072 nt
	global_load_dwordx2 v[214:215], v[150:151], off offset:3584 nt
	s_mov_b32 s4, 0x3e000000
	v_add_co_u32_e64 v122, s[38:39], s80, v122
	s_add_i32 s25, s25, s66
	s_nop 0
	v_addc_co_u32_e64 v123, s[38:39], 0, v123, s[38:39]
	v_lshl_add_u64 v[86:87], v[86:87], 0, s[22:23]
	v_lshl_add_u64 v[88:89], v[88:89], 0, s[94:95]
	s_waitcnt vmcnt(8)
	v_readfirstlane_b32 s5, v126
	v_readfirstlane_b32 s6, v127
	s_nop 0
	v_pk_mul_f32 v[126:127], v[128:129], s[4:5] op_sel_hi:[1,0]
	s_lshr_b32 s4, s5, 18
	s_lshl_b32 s5, s5, 11
	s_lshr_b32 s7, s6, 18
	s_and_b32 s4, s4, 0x3ffc
	s_and_b32 s20, s5, 0x7ffff800
	s_and_b32 s5, s7, 0x3ffc
	s_add_i32 s4, s81, s4
	s_add_i32 s5, s81, s5
	v_mov_b32_e32 v128, s4
	v_mov_b32_e32 v129, s5
	ds_read_b32 v128, v128
	ds_read_b32 v130, v129
	s_lshl_b32 s6, s6, 11
	s_waitcnt lgkmcnt(1)
	v_ashrrev_i32_e32 v129, 31, v128
	v_lshlrev_b64 v[128:129], 19, v[128:129]
	v_lshl_add_u64 v[128:129], s[48:49], 0, v[128:129]
	v_lshl_add_u64 v[128:129], v[128:129], 0, s[20:21]
	s_waitcnt lgkmcnt(0)
	v_ashrrev_i32_e32 v131, 31, v130
	v_readfirstlane_b32 s4, v128
	v_readfirstlane_b32 s5, v129
	v_lshlrev_b64 v[130:131], 19, v[130:131]
	v_lshl_add_u64 v[130:131], s[48:49], 0, v[130:131]
	s_and_b32 s20, s6, 0x7ffff800
	v_lshl_add_u64 v[130:131], v[130:131], 0, s[20:21]
	s_add_u32 s29, s29, s68
	global_load_dword v129, v170, s[4:5] nt
	v_readfirstlane_b32 s6, v130
	v_readfirstlane_b32 s7, v131
	global_load_dword v131, v170, s[4:5] offset:256 nt
	global_load_dword v145, v170, s[4:5] offset:512 nt
	global_load_dword v154, v170, s[4:5] offset:768 nt
	global_load_dword v156, v170, s[4:5] offset:1024 nt
	global_load_dword v158, v170, s[4:5] offset:1280 nt
	global_load_dword v159, v170, s[4:5] offset:1536 nt
	global_load_dword v160, v170, s[4:5] offset:1792 nt
	global_load_dword v133, v170, s[6:7] nt
	global_load_dword v141, v170, s[6:7] offset:256 nt
	global_load_dword v149, v170, s[6:7] offset:512 nt
	global_load_dword v157, v170, s[6:7] offset:768 nt
	global_load_dword v161, v170, s[6:7] offset:1024 nt
	global_load_dword v162, v170, s[6:7] offset:1280 nt
	global_load_dword v163, v170, s[6:7] offset:1536 nt
	global_load_dword v171, v170, s[6:7] offset:1792 nt
	s_addc_u32 s52, s52, s69
	s_cmp_ge_i32 s25, s28
	s_waitcnt vmcnt(14)
	v_cvt_f32_fp8_e32 v136, v131
	v_cvt_f32_fp8_sdwa v138, v131 src0_sel:BYTE_1
	v_cvt_f32_fp8_sdwa v140, v131 src0_sel:BYTE_2
	v_cvt_f32_fp8_sdwa v142, v131 src0_sel:BYTE_3
	s_waitcnt vmcnt(13)
	v_cvt_f32_fp8_sdwa v146, v145 src0_sel:BYTE_1
	v_cvt_f32_fp8_e32 v144, v145
	v_cvt_f32_fp8_sdwa v148, v145 src0_sel:BYTE_2
	s_waitcnt vmcnt(7)
	v_cvt_f32_fp8_e32 v131, v133
	v_cvt_f32_fp8_sdwa v135, v133 src0_sel:BYTE_2
	s_waitcnt vmcnt(6)
	v_cvt_f32_fp8_e32 v139, v141
	v_cvt_f32_fp8_sdwa v137, v141 src0_sel:BYTE_1
	v_cvt_f32_fp8_sdwa v130, v129 src0_sel:BYTE_1
	v_cvt_f32_fp8_sdwa v134, v129 src0_sel:BYTE_3
	v_cvt_f32_fp8_e32 v128, v129
	v_cvt_f32_fp8_sdwa v132, v129 src0_sel:BYTE_2
	v_cvt_f32_fp8_sdwa v129, v133 src0_sel:BYTE_1
	v_cvt_f32_fp8_sdwa v133, v133 src0_sel:BYTE_3
	s_waitcnt vmcnt(5)
	v_cvt_f32_fp8_e32 v147, v149
	v_cvt_f32_fp8_sdwa v143, v141 src0_sel:BYTE_2
	v_cvt_f32_fp8_sdwa v152, v145 src0_sel:BYTE_3
	v_cvt_f32_fp8_sdwa v145, v149 src0_sel:BYTE_1
	v_cvt_f32_fp8_sdwa v141, v141 src0_sel:BYTE_3
	v_pk_mul_f32 v[130:131], v[126:127], v[130:131]
	v_pk_mul_f32 v[134:135], v[126:127], v[134:135]
	v_pk_mul_f32 v[138:139], v[126:127], v[138:139]
	v_pk_fma_f32 v[128:129], v[126:127], v[128:129], v[130:131] op_sel:[0,0,1] op_sel_hi:[1,1,0]
	v_cvt_f32_fp8_e32 v130, v154
	v_pk_fma_f32 v[132:133], v[126:127], v[132:133], v[134:135] op_sel:[0,0,1] op_sel_hi:[1,1,0]
	v_cvt_f32_fp8_sdwa v134, v154 src0_sel:BYTE_1
	v_pk_fma_f32 v[136:137], v[126:127], v[136:137], v[138:139] op_sel:[0,0,1] op_sel_hi:[1,1,0]
	v_cvt_f32_fp8_sdwa v138, v154 src0_sel:BYTE_2
	v_cvt_f32_fp8_sdwa v154, v154 src0_sel:BYTE_3
	s_waitcnt vmcnt(4)
	v_cvt_f32_fp8_sdwa v155, v157 src0_sel:BYTE_2
	v_pk_mul_f32 v[146:147], v[126:127], v[146:147]
	v_cvt_f32_fp8_e32 v135, v157
	v_cvt_f32_fp8_sdwa v139, v157 src0_sel:BYTE_3
	v_pk_mul_f32 v[142:143], v[126:127], v[142:143]
	v_pk_fma_f32 v[144:145], v[126:127], v[144:145], v[146:147] op_sel:[0,0,1] op_sel_hi:[1,1,0]
	v_cvt_f32_fp8_sdwa v146, v156 src0_sel:BYTE_1
	v_cvt_f32_fp8_sdwa v131, v157 src0_sel:BYTE_1
	s_waitcnt vmcnt(3)
	v_cvt_f32_fp8_e32 v147, v161
	v_cvt_f32_fp8_sdwa v153, v149 src0_sel:BYTE_2
	v_pk_fma_f32 v[140:141], v[126:127], v[140:141], v[142:143] op_sel:[0,0,1] op_sel_hi:[1,1,0]
	v_cvt_f32_fp8_e32 v142, v156
	v_cvt_f32_fp8_sdwa v143, v161 src0_sel:BYTE_1
	v_cvt_f32_fp8_sdwa v149, v149 src0_sel:BYTE_3
	v_pk_mul_f32 v[154:155], v[126:127], v[154:155]
	v_pk_mul_f32 v[134:135], v[126:127], v[134:135]
	v_pk_fma_f32 v[172:173], v[126:127], v[138:139], v[154:155] op_sel:[0,0,1] op_sel_hi:[1,1,0]
	v_cvt_f32_fp8_sdwa v138, v158 src0_sel:BYTE_1
	s_waitcnt vmcnt(2)
	v_cvt_f32_fp8_e32 v139, v162
	v_pk_fma_f32 v[134:135], v[126:127], v[130:131], v[134:135] op_sel:[0,0,1] op_sel_hi:[1,1,0]
	v_cvt_f32_fp8_e32 v130, v158
	v_pk_mul_f32 v[146:147], v[126:127], v[146:147]
	v_cvt_f32_fp8_sdwa v154, v158 src0_sel:BYTE_3
	v_cvt_f32_fp8_sdwa v131, v162 src0_sel:BYTE_1
	v_cvt_f32_fp8_sdwa v155, v162 src0_sel:BYTE_2
	v_pk_mul_f32 v[152:153], v[126:127], v[152:153]
	v_pk_fma_f32 v[146:147], v[126:127], v[142:143], v[146:147] op_sel:[0,0,1] op_sel_hi:[1,1,0]
	v_cvt_f32_fp8_sdwa v142, v158 src0_sel:BYTE_2
	v_cvt_f32_fp8_sdwa v143, v162 src0_sel:BYTE_3
	v_pk_fma_f32 v[148:149], v[126:127], v[148:149], v[152:153] op_sel:[0,0,1] op_sel_hi:[1,1,0]
	v_cvt_f32_fp8_sdwa v152, v156 src0_sel:BYTE_2
	v_cvt_f32_fp8_sdwa v156, v156 src0_sel:BYTE_3
	v_cvt_f32_fp8_sdwa v157, v161 src0_sel:BYTE_2
	v_cvt_f32_fp8_sdwa v153, v161 src0_sel:BYTE_3
	v_pk_mul_f32 v[138:139], v[126:127], v[138:139]
	v_pk_mul_f32 v[156:157], v[126:127], v[156:157]
	v_pk_fma_f32 v[176:177], v[126:127], v[130:131], v[138:139] op_sel:[0,0,1] op_sel_hi:[1,1,0]
	v_pk_mul_f32 v[138:139], v[126:127], v[154:155]
	v_cvt_f32_fp8_sdwa v130, v159 src0_sel:BYTE_1
	v_pk_fma_f32 v[178:179], v[126:127], v[142:143], v[138:139] op_sel:[0,0,1] op_sel_hi:[1,1,0]
	v_cvt_f32_fp8_sdwa v142, v159 src0_sel:BYTE_3
	s_waitcnt vmcnt(1)
	v_cvt_f32_fp8_sdwa v143, v163 src0_sel:BYTE_2
	v_cvt_f32_fp8_sdwa v138, v159 src0_sel:BYTE_2
	v_cvt_f32_fp8_e32 v131, v163
	v_cvt_f32_fp8_sdwa v139, v163 src0_sel:BYTE_3
	v_pk_fma_f32 v[174:175], v[126:127], v[152:153], v[156:157] op_sel:[0,0,1] op_sel_hi:[1,1,0]
	v_cvt_f32_fp8_e32 v152, v159
	v_cvt_f32_fp8_sdwa v153, v163 src0_sel:BYTE_1
	v_pk_mul_f32 v[142:143], v[126:127], v[142:143]
	v_pk_mul_f32 v[130:131], v[126:127], v[130:131]
	v_pk_fma_f32 v[180:181], v[126:127], v[138:139], v[142:143] op_sel:[0,0,1] op_sel_hi:[1,1,0]
	v_cvt_f32_fp8_sdwa v138, v160 src0_sel:BYTE_1
	s_waitcnt vmcnt(0)
	v_cvt_f32_fp8_e32 v139, v171
	v_pk_fma_f32 v[154:155], v[126:127], v[152:153], v[130:131] op_sel:[0,0,1] op_sel_hi:[1,1,0]
	v_cvt_f32_fp8_e32 v130, v160
	v_cvt_f32_fp8_sdwa v131, v171 src0_sel:BYTE_1
	v_pk_mul_f32 v[138:139], v[126:127], v[138:139]
	v_lshlrev_b32_e32 v142, 16, v124
	v_and_b32_e32 v143, 0xffff0000, v124
	v_pk_fma_f32 v[152:153], v[126:127], v[130:131], v[138:139] op_sel:[0,0,1] op_sel_hi:[1,1,0]
	v_cvt_f32_fp8_sdwa v138, v160 src0_sel:BYTE_3
	v_cvt_f32_fp8_sdwa v139, v171 src0_sel:BYTE_2
	v_cvt_f32_fp8_sdwa v130, v160 src0_sel:BYTE_2
	v_cvt_f32_fp8_sdwa v131, v171 src0_sel:BYTE_3
	v_lshlrev_b32_e32 v124, 16, v125
	v_pk_mul_f32 v[138:139], v[126:127], v[138:139]
	v_and_b32_e32 v125, 0xffff0000, v125
	v_pk_fma_f32 v[156:157], v[126:127], v[130:131], v[138:139] op_sel:[0,0,1] op_sel_hi:[1,1,0]
	v_pk_fma_f32 v[124:125], v[8:9], v[132:133], v[124:125]
	v_and_b32_e32 v171, 64, v226
	v_lshlrev_b32_e32 v182, 16, v202
	v_and_b32_e32 v183, 0xffff0000, v202
	v_lshlrev_b32_e32 v186, 16, v206
	v_and_b32_e32 v187, 0xffff0000, v206
	v_lshlrev_b32_e32 v188, 16, v207
	v_and_b32_e32 v189, 0xffff0000, v207
	v_lshlrev_b32_e32 v126, 16, v203
	v_and_b32_e32 v127, 0xffff0000, v203
	v_lshlrev_b32_e32 v184, 16, v204
	v_and_b32_e32 v185, 0xffff0000, v204
	v_lshlrev_b32_e32 v130, 16, v205
	v_and_b32_e32 v131, 0xffff0000, v205
	v_pk_fma_f32 v[126:127], v[16:17], v[140:141], v[126:127]
	v_pk_fma_f32 v[140:141], v[14:15], v[136:137], v[182:183]
	v_lshlrev_b32_e32 v192, 16, v208
	v_lshlrev_b32_e32 v196, 16, v210
	v_and_b32_e32 v197, 0xffff0000, v210
	v_lshlrev_b32_e32 v198, 16, v211
	v_and_b32_e32 v199, 0xffff0000, v211
	v_lshlrev_b32_e32 v158, 16, v214
	v_and_b32_e32 v159, 0xffff0000, v214
	v_and_b32_e32 v193, 0xffff0000, v208
	v_lshlrev_b32_e32 v194, 16, v209
	v_and_b32_e32 v195, 0xffff0000, v209
	v_pk_fma_f32 v[138:139], v[6:7], v[128:129], v[142:143]
	v_pk_fma_f32 v[158:159], v[62:63], v[152:153], v[158:159]
	v_cvt_pk_bf16_f32 v152, v138, v139
	v_cvt_pk_bf16_f32 v153, v124, v125
	global_store_dwordx2 v[150:151], v[152:153], off
	v_cvt_pk_bf16_f32 v152, v140, v141
	v_cvt_pk_bf16_f32 v153, v126, v127
	v_pk_fma_f32 v[128:129], v[24:25], v[148:149], v[130:131]
	v_pk_fma_f32 v[142:143], v[22:23], v[144:145], v[184:185]
	global_store_dwordx2 v[150:151], v[152:153], off offset:512
	v_cvt_pk_bf16_f32 v152, v142, v143
	v_cvt_pk_bf16_f32 v153, v128, v129
	v_pk_fma_f32 v[130:131], v[32:33], v[172:173], v[188:189]
	v_pk_fma_f32 v[144:145], v[30:31], v[134:135], v[186:187]
	global_store_dwordx2 v[150:151], v[152:153], off offset:1024
	v_cvt_pk_bf16_f32 v152, v144, v145
	v_cvt_pk_bf16_f32 v153, v130, v131
	v_pk_fma_f32 v[132:133], v[40:41], v[174:175], v[194:195]
	v_pk_fma_f32 v[146:147], v[38:39], v[146:147], v[192:193]
	global_store_dwordx2 v[150:151], v[152:153], off offset:1536
	v_cvt_pk_bf16_f32 v152, v146, v147
	v_cvt_pk_bf16_f32 v153, v132, v133
	v_lshlrev_b32_e32 v162, 16, v212
	v_and_b32_e32 v163, 0xffff0000, v212
	v_lshlrev_b32_e32 v200, 16, v213
	v_and_b32_e32 v201, 0xffff0000, v213
	v_lshlrev_b32_e32 v160, 16, v215
	v_and_b32_e32 v161, 0xffff0000, v215
	v_pk_fma_f32 v[134:135], v[48:49], v[178:179], v[198:199]
	v_pk_fma_f32 v[148:149], v[46:47], v[176:177], v[196:197]
	global_store_dwordx2 v[150:151], v[152:153], off offset:2048
	v_cvt_pk_bf16_f32 v152, v148, v149
	v_cvt_pk_bf16_f32 v153, v134, v135
	v_pk_fma_f32 v[136:137], v[56:57], v[180:181], v[200:201]
	v_pk_fma_f32 v[154:155], v[54:55], v[154:155], v[162:163]
	v_xor_b32_e32 v163, 1, v226
	v_xor_b32_e32 v172, 2, v226
	v_pk_fma_f32 v[156:157], v[64:65], v[156:157], v[160:161]
	v_xor_b32_e32 v173, 4, v226
	v_xor_b32_e32 v174, 8, v226
	v_add_u32_e32 v160, 64, v171
	global_store_dwordx2 v[150:151], v[152:153], off offset:2560
	v_cvt_pk_bf16_f32 v152, v154, v155
	v_cvt_pk_bf16_f32 v153, v136, v137
	v_cmp_lt_i32_e32 vcc, v163, v160
	v_cmp_lt_i32_e64 s[38:39], v172, v160
	v_cmp_lt_i32_e64 s[40:41], v173, v160
	v_cmp_lt_i32_e64 s[42:43], v174, v160
	v_mul_f32_e32 v160, v139, v139
	global_store_dwordx2 v[150:151], v[152:153], off offset:3072
	v_cvt_pk_bf16_f32 v152, v158, v159
	v_cvt_pk_bf16_f32 v153, v156, v157
	global_store_dwordx2 v[150:151], v[152:153], off offset:3584
	v_mul_f32_e32 v150, v125, v125
	v_fmac_f32_e32 v160, v138, v138
	v_fmac_f32_e32 v150, v124, v124
	v_mul_f32_e32 v151, v141, v141
	v_mul_f32_e32 v152, v127, v127
	v_mul_f32_e32 v153, v143, v143
	v_add_f32_e32 v150, v160, v150
	v_mul_f32_e32 v160, v129, v129
	v_fmac_f32_e32 v151, v140, v140
	v_fmac_f32_e32 v152, v126, v126
	v_fmac_f32_e32 v153, v142, v142
	v_fmac_f32_e32 v160, v128, v128
	v_add_f32_e32 v151, v151, v152
	v_mul_f32_e32 v152, v145, v145
	v_add_f32_e32 v153, v153, v160
	v_mul_f32_e32 v160, v131, v131
	v_fmac_f32_e32 v152, v144, v144
	v_fmac_f32_e32 v160, v130, v130
	v_add_f32_e32 v152, v152, v160
	v_mul_f32_e32 v160, v147, v147
	v_mul_f32_e32 v161, v133, v133
	v_fmac_f32_e32 v160, v146, v146
	v_fmac_f32_e32 v161, v132, v132
	v_add_f32_e32 v160, v160, v161
	v_mul_f32_e32 v161, v149, v149
	v_mul_f32_e32 v162, v135, v135
	v_fmac_f32_e32 v161, v148, v148
	v_fmac_f32_e32 v162, v134, v134
	v_add_f32_e32 v150, v150, v151
	v_add_f32_e32 v161, v161, v162
	v_mul_f32_e32 v162, v155, v155
	v_mul_f32_e32 v171, v137, v137
	v_add_f32_e32 v150, v150, v153
	v_fmac_f32_e32 v162, v154, v154
	v_fmac_f32_e32 v171, v136, v136
	v_add_f32_e32 v150, v150, v152
	v_add_f32_e32 v162, v162, v171
	v_mul_f32_e32 v171, v159, v159
	v_mul_f32_e32 v175, v157, v157
	v_add_f32_e32 v150, v150, v160
	v_fmac_f32_e32 v171, v158, v158
	v_fmac_f32_e32 v175, v156, v156
	v_add_f32_e32 v150, v150, v161
	v_add_f32_e32 v171, v171, v175
	v_add_f32_e32 v150, v150, v162
	v_cndmask_b32_e32 v151, v226, v163, vcc
	v_lshlrev_b32_e32 v151, 2, v151
	v_add_f32_e32 v150, v150, v171
	ds_bpermute_b32 v151, v151, v150
	v_cndmask_b32_e64 v152, v226, v172, s[38:39]
	v_lshlrev_b32_e32 v152, 2, v152
	v_cndmask_b32_e64 v153, v226, v173, s[40:41]
	v_lshlrev_b32_e32 v153, 2, v153
	s_waitcnt lgkmcnt(0)
	v_add_f32_e32 v150, v150, v151
	ds_bpermute_b32 v151, v152, v150
	v_cndmask_b32_e64 v163, v226, v174, s[42:43]
	v_lshlrev_b32_e32 v163, 2, v163
	v_mov_b32_e32 v160, 0
	v_mov_b32_e32 v161, 0
	s_waitcnt lgkmcnt(0)
	v_add_f32_e32 v150, v150, v151
	ds_bpermute_b32 v151, v153, v150
	v_mov_b32_e32 v162, 0
	v_mov_b32_e32 v173, 0
	s_waitcnt lgkmcnt(0)
	v_add_f32_e32 v150, v150, v151
	ds_bpermute_b32 v151, v163, v150
	s_waitcnt lgkmcnt(0)
	v_add_f32_e32 v150, v150, v151
	v_mov_b32_e32 v151, v150
	s_nop 1
	v_permlane16_swap_b32_e32 v150, v151
	v_add_f32_e32 v150, v150, v151
	v_mov_b32_e32 v151, v150
	s_nop 1
	v_permlane32_swap_b32_e32 v150, v151
	v_add_f32_e32 v150, v150, v151
	v_fmamk_f32 v150, v150, 0x3a000000, v228
	v_mul_f32_e32 v151, 0x4f800000, v150
	v_cmp_gt_f32_e32 vcc, s82, v150
	s_nop 1
	v_cndmask_b32_e32 v150, v150, v151, vcc
	v_sqrt_f32_e32 v151, v150
	s_nop 0
	v_add_u32_e32 v152, -1, v151
	v_add_u32_e32 v153, 1, v151
	v_fma_f32 v163, -v152, v151, v150
	v_fma_f32 v171, -v153, v151, v150
	v_cmp_ge_f32_e64 s[38:39], 0, v163
	s_nop 1
	v_cndmask_b32_e64 v151, v151, v152, s[38:39]
	v_cmp_lt_f32_e64 s[38:39], 0, v171
	v_mov_b32_e32 v171, 0
	s_nop 0
	v_cndmask_b32_e64 v151, v151, v153, s[38:39]
	v_mul_f32_e32 v152, 0x37800000, v151
	v_cndmask_b32_e32 v151, v151, v152, vcc
	v_cmp_class_f32_e32 vcc, v150, v229
	s_nop 1
	v_cndmask_b32_e32 v150, v151, v150, vcc
	v_div_scale_f32 v151, s[4:5], v150, v150, 1.0
	v_rcp_f32_e32 v153, v151
	v_div_scale_f32 v152, vcc, 1.0, v150, 1.0
	v_fma_f32 v163, -v151, v153, 1.0
	v_fmac_f32_e32 v153, v163, v153
	v_mul_f32_e32 v172, v152, v153
	v_fma_f32 v163, -v151, v172, v152
	v_fmac_f32_e32 v172, v163, v153
	v_fma_f32 v151, -v151, v172, v152
	v_div_fmas_f32 v151, v151, v153, v172
	v_div_fixup_f32 v174, v151, v150, 1.0
	v_pk_mul_f32 v[138:139], v[138:139], v[174:175] op_sel_hi:[1,0]
	v_pk_mul_f32 v[150:151], v[124:125], v[174:175] op_sel_hi:[1,0]
	v_pk_mul_f32 v[124:125], v[140:141], v[174:175] op_sel_hi:[1,0]
	v_pk_fma_f32 v[138:139], v[92:93], v[138:139], v[2:3]
	v_pk_mul_f32 v[140:141], v[126:127], v[174:175] op_sel_hi:[1,0]
	v_pk_mul_f32 v[126:127], v[142:143], v[174:175] op_sel_hi:[1,0]
	v_pk_fma_f32 v[124:125], v[96:97], v[124:125], v[10:11]
	v_med3_f32 v138, v138, s33, v233
	v_med3_f32 v139, v139, s33, v233
	v_pk_mul_f32 v[142:143], v[128:129], v[174:175] op_sel_hi:[1,0]
	v_pk_mul_f32 v[128:129], v[144:145], v[174:175] op_sel_hi:[1,0]
	v_pk_fma_f32 v[126:127], v[100:101], v[126:127], v[18:19]
	v_med3_f32 v124, v124, s33, v233
	v_med3_f32 v125, v125, s33, v233
	v_cvt_pk_fp8_f32 v160, v138, v139
	v_pk_mul_f32 v[144:145], v[130:131], v[174:175] op_sel_hi:[1,0]
	v_pk_mul_f32 v[130:131], v[146:147], v[174:175] op_sel_hi:[1,0]
	v_pk_mul_f32 v[146:147], v[132:133], v[174:175] op_sel_hi:[1,0]
	v_pk_mul_f32 v[132:133], v[148:149], v[174:175] op_sel_hi:[1,0]
	v_pk_mul_f32 v[148:149], v[134:135], v[174:175] op_sel_hi:[1,0]
	v_pk_mul_f32 v[134:135], v[154:155], v[174:175] op_sel_hi:[1,0]
	v_pk_mul_f32 v[152:153], v[136:137], v[174:175] op_sel_hi:[1,0]
	v_pk_mul_f32 v[136:137], v[158:159], v[174:175] op_sel_hi:[1,0]
	v_pk_fma_f32 v[128:129], v[104:105], v[128:129], v[26:27]
	v_med3_f32 v126, v126, s33, v233
	v_med3_f32 v127, v127, s33, v233
	v_cvt_pk_fp8_f32 v161, v124, v125
	v_mov_b32_e32 v163, 0
	v_pk_fma_f32 v[150:151], v[90:91], v[150:151], v[4:5]
	v_pk_fma_f32 v[130:131], v[108:109], v[130:131], v[34:35]
	v_pk_fma_f32 v[132:133], v[112:113], v[132:133], v[42:43]
	v_pk_fma_f32 v[134:135], v[116:117], v[134:135], v[50:51]
	v_pk_fma_f32 v[136:137], v[120:121], v[136:137], v[58:59]
	v_med3_f32 v128, v128, s33, v233
	v_med3_f32 v129, v129, s33, v233
	v_cvt_pk_fp8_f32 v162, v126, v127
	v_mov_b32_e32 v172, 0
	v_pk_mul_f32 v[154:155], v[156:157], v[174:175] op_sel_hi:[1,0]
	v_mov_b32_e32 v156, 0
	v_pk_fma_f32 v[140:141], v[94:95], v[140:141], v[12:13]
	v_med3_f32 v150, v150, s33, v233
	v_med3_f32 v151, v151, s33, v233
	v_med3_f32 v130, v130, s33, v233
	v_med3_f32 v131, v131, s33, v233
	v_med3_f32 v132, v132, s33, v233
	v_med3_f32 v133, v133, s33, v233
	v_med3_f32 v134, v134, s33, v233
	v_med3_f32 v135, v135, s33, v233
	v_med3_f32 v136, v136, s33, v233
	v_med3_f32 v137, v137, s33, v233
	v_cvt_pk_fp8_f32 v163, v128, v129
	v_pk_fma_f32 v[142:143], v[98:99], v[142:143], v[20:21]
	v_med3_f32 v140, v140, s33, v233
	v_med3_f32 v141, v141, s33, v233
	v_cvt_pk_fp8_f32 v171, v130, v131
	v_cvt_pk_fp8_f32 v172, v132, v133
	v_cvt_pk_fp8_f32 v173, v134, v135
	v_cvt_pk_fp8_f32 v156, v136, v137
	v_cvt_pk_fp8_f32 v160, v150, v151 op_sel:[0,0,1]
	v_pk_fma_f32 v[144:145], v[102:103], v[144:145], v[28:29]
	v_med3_f32 v142, v142, s33, v233
	v_med3_f32 v143, v143, s33, v233
	v_cvt_pk_fp8_f32 v161, v140, v141 op_sel:[0,0,1]
	v_pk_fma_f32 v[146:147], v[106:107], v[146:147], v[36:37]
	v_pk_fma_f32 v[148:149], v[110:111], v[148:149], v[44:45]
	v_pk_fma_f32 v[152:153], v[114:115], v[152:153], v[52:53]
	v_pk_fma_f32 v[154:155], v[118:119], v[154:155], v[60:61]
	v_med3_f32 v144, v144, s33, v233
	v_med3_f32 v145, v145, s33, v233
	v_cvt_pk_fp8_f32 v162, v142, v143 op_sel:[0,0,1]
	v_med3_f32 v146, v146, s33, v233
	v_med3_f32 v147, v147, s33, v233
	v_med3_f32 v148, v148, s33, v233
	v_med3_f32 v149, v149, s33, v233
	v_med3_f32 v152, v152, s33, v233
	v_med3_f32 v153, v153, s33, v233
	v_med3_f32 v154, v154, s33, v233
	v_med3_f32 v155, v155, s33, v233
	v_cvt_pk_fp8_f32 v163, v144, v145 op_sel:[0,0,1]
	v_cvt_pk_fp8_f32 v171, v146, v147 op_sel:[0,0,1]
	v_cvt_pk_fp8_f32 v172, v148, v149 op_sel:[0,0,1]
	v_cvt_pk_fp8_f32 v173, v152, v153 op_sel:[0,0,1]
	v_cvt_pk_fp8_f32 v156, v154, v155 op_sel:[0,0,1]
	global_store_dword v[122:123], v160, off
	global_store_dword v[122:123], v161, off offset:256
	global_store_dword v[122:123], v162, off offset:512
	global_store_dword v[122:123], v163, off offset:768
	global_store_dword v[122:123], v171, off offset:1024
	global_store_dword v[122:123], v172, off offset:1280
	global_store_dword v[122:123], v173, off offset:1536
	global_store_dword v[122:123], v156, off offset:1792
	s_cbranch_scc0 .LBB0_256
	s_branch .LBB0_253
